# speedup vs baseline: 1.0025x; 1.0025x over previous
_Z9proj_gemmPKfS0_S0_PK14__hip_bfloat16S0_S0_S0_PS1_:
	v_readfirstlane_b32 s40, v0
	s_nop 3
	s_lshr_b32 s40, s40, 8
	s_cmp_lg_u32 s40, 0
	s_cbranch_scc0 .Lprio_done
	s_setprio 1
.Lprio_done:
	s_lshl_b32 s3, s2, 2
	s_load_dwordx8 s[8:15], s[0:1], 0x0
	s_and_b32 s3, s3, 28
	s_bfe_u32 s30, s2, 0x20005
	s_lshr_b32 s6, s2, 3
	s_ashr_i32 s18, s2, 7
	s_lshr_b32 s7, s2, 5
	s_or_b32 s20, s3, s30
	s_bfe_u32 s3, s2, 0x20003
	s_cmpk_lt_u32 s2, 0x80
	s_cselect_b64 s[16:17], -1, 0
	s_and_b64 s[4:5], s[16:17], exec
	s_waitcnt lgkmcnt(0)
	s_cselect_b32 s4, s9, s11
	s_cselect_b32 s5, s8, s10
	s_lshl_b32 s24, s20, 18
	s_lshl_b32 s8, s20, 20
	s_add_u32 s25, s5, s8
	s_addc_u32 s26, s4, 0
	s_ashr_i32 s19, s18, 31
	s_lshl_b64 s[4:5], s[18:19], 21
	s_add_u32 s4, s14, s4
	s_addc_u32 s5, s15, s5
	s_lshl_b32 s8, s3, 19
	s_add_u32 s27, s4, s8
	s_addc_u32 s28, s5, 0
	s_xor_b32 s6, s6, s18
	v_lshlrev_b32_e32 v1, 4, v0
	s_lshl_b32 s34, s6, 4
	v_lshlrev_b32_e32 v2, 3, v0
	v_and_b32_e32 v3, 0x1f0, v1
	s_movk_i32 s6, 0x200
	s_lshl_b32 s4, s20, 1
	s_mul_i32 s31, s18, 5
	s_xor_b32 s7, s7, s18
	v_lshrrev_b32_e32 v28, 6, v0
	s_and_b32 s35, s34, 16
	v_and_or_b32 v29, v2, s6, v3
	v_lshrrev_b32_e32 v2, 1, v0
	v_and_b32_e32 v3, 48, v1
	s_add_i32 s4, s4, s31
	v_bitop3_b32 v2, v2, v3, 32 bitop3:0x6c
	v_or_b32_e32 v30, s35, v28
	s_lshl_b32 s38, s7, 4
	s_and_b32 s5, s4, 15
	v_lshrrev_b32_e32 v2, 1, v2
	v_or_b32_e32 v32, 8, v30
	s_and_b32 s39, s38, 16
	v_and_or_b32 v178, v0, 32, v2
	v_lshlrev_b32_e32 v2, 3, v30
	v_lshrrev_b32_e32 v31, 6, v29
	s_movk_i32 s36, 0xb0
	v_lshlrev_b32_e32 v3, 3, v32
	s_movk_i32 s37, 0xf0
	v_or_b32_e32 v33, s39, v28
	s_lshl_b32 s33, s4, 6
	s_lshl_b32 s4, s5, 8
	v_and_or_b32 v2, v2, s36, v31
	v_and_or_b32 v12, v3, s37, v31
	v_lshlrev_b32_e32 v3, 3, v33
	v_or_b32_e32 v34, 8, v33
	s_add_u32 s20, s25, s4
	v_mov_b32_e32 v183, 0
	v_and_or_b32 v20, v3, s36, v31
	v_lshlrev_b32_e32 v3, 3, v34
	s_addc_u32 s21, s26, 0
	v_lshlrev_b32_e32 v180, 12, v2
	v_mov_b32_e32 v181, v183
	v_and_or_b32 v22, v3, s37, v31
	v_lshl_add_u64 v[2:3], s[20:21], 0, v[180:181]
	v_lshlrev_b32_e32 v182, 2, v178
	v_lshl_add_u64 v[10:11], v[2:3], 0, v[182:183]
	v_lshlrev_b32_e32 v184, 12, v12
	v_mov_b32_e32 v185, v183
	s_lshl_b32 s4, s5, 7
	global_load_dwordx4 v[2:5], v[10:11], off offset:16
	global_load_dwordx4 v[6:9], v[10:11], off
	v_lshl_add_u64 v[10:11], s[20:21], 0, v[184:185]
	s_add_u32 s22, s27, s4
	v_lshl_add_u64 v[14:15], v[10:11], 0, v[182:183]
	s_addc_u32 s23, s28, 0
	v_lshlrev_b32_e32 v186, 11, v20
	v_mov_b32_e32 v187, v183
	global_load_dwordx4 v[10:13], v[14:15], off offset:16
	global_load_dwordx4 v[16:19], v[14:15], off
	v_lshl_add_u64 v[20:21], s[22:23], 0, v[186:187]
	v_lshlrev_b32_e32 v14, 1, v178
	v_mov_b32_e32 v15, v183
	v_lshlrev_b32_e32 v188, 11, v22
	v_mov_b32_e32 v189, v183
	v_lshl_add_u64 v[24:25], v[20:21], 0, v[14:15]
	v_lshl_add_u64 v[20:21], s[22:23], 0, v[188:189]
	v_lshl_add_u64 v[26:27], v[20:21], 0, v[14:15]
	global_load_dwordx4 v[20:23], v[24:25], off
	global_load_dwordx4 v[50:53], v[26:27], off
	v_bfe_u32 v24, v0, 5, 1
	v_and_or_b32 v25, v30, 22, v24
	v_lshl_or_b32 v208, v25, 10, v29
	v_and_or_b32 v25, v32, 30, v24
	v_lshl_or_b32 v205, v25, 10, v29
	v_bitop3_b32 v25, s34, 16, v28 bitop3:0x26
	v_and_or_b32 v26, v25, 22, v24
	v_lshl_or_b32 v204, v26, 10, v29
	v_bitop3_b32 v26, s35, v28, 24 bitop3:0xde
	v_and_or_b32 v27, v26, 30, v24
	v_lshl_or_b32 v201, v27, 10, v29
	v_and_or_b32 v27, v33, 22, v24
	v_lshl_or_b32 v206, v27, 10, v29
	v_and_or_b32 v27, v34, 30, v24
	s_load_dwordx8 s[4:11], s[0:1], 0x20
	v_lshl_or_b32 v207, v27, 10, v29
	v_bitop3_b32 v27, s38, 16, v28 bitop3:0x26
	v_bitop3_b32 v28, s39, v28, 24 bitop3:0xde
	v_and_or_b32 v30, v27, 22, v24
	v_and_or_b32 v24, v28, 30, v24
	v_and_b32_e32 v179, 15, v0
	v_lshl_or_b32 v202, v30, 10, v29
	v_lshl_or_b32 v203, v24, 10, v29
	v_lshlrev_b32_e32 v24, 3, v28
	v_lshlrev_b32_e32 v29, 2, v0
	v_lshrrev_b32_e32 v198, 8, v0
	v_lshlrev_b32_e32 v25, 3, v25
	v_lshlrev_b32_e32 v26, 3, v26
	v_lshlrev_b32_e32 v27, 3, v27
	v_and_or_b32 v28, v24, s37, v31
	v_and_b32_e32 v24, 48, v0
	v_and_b32_e32 v29, 32, v29
	v_lshlrev_b32_e32 v30, 6, v179
	s_mov_b32 s29, 0
	v_and_b32_e32 v199, 63, v0
	v_and_or_b32 v25, v25, s36, v31
	v_and_or_b32 v26, v26, s37, v31
	v_bfe_u32 v200, v0, 6, 2
	v_and_or_b32 v27, v27, s36, v31
	v_lshlrev_b32_e32 v80, 14, v198
	v_bitop3_b32 v81, v30, v29, v24 bitop3:0x36
	v_lshlrev_b32_e32 v190, 12, v25
	v_mov_b32_e32 v191, v183
	v_lshl_add_u64 v[24:25], s[20:21], 0, v[190:191]
	v_lshl_add_u64 v[24:25], v[24:25], 0, v[182:183]
	v_lshlrev_b32_e32 v192, 12, v26
	v_mov_b32_e32 v193, v183
	global_load_dwordx4 v[54:57], v[24:25], off offset:16
	global_load_dwordx4 v[58:61], v[24:25], off
	v_lshl_add_u64 v[24:25], s[20:21], 0, v[192:193]
	v_lshl_add_u64 v[24:25], v[24:25], 0, v[182:183]
	v_lshlrev_b32_e32 v194, 11, v27
	v_mov_b32_e32 v195, v183
	global_load_dwordx4 v[62:65], v[24:25], off offset:16
	global_load_dwordx4 v[66:69], v[24:25], off
	v_lshl_add_u64 v[24:25], s[22:23], 0, v[194:195]
	v_lshlrev_b32_e32 v196, 11, v28
	v_mov_b32_e32 v197, v183
	v_lshl_add_u64 v[24:25], v[24:25], 0, v[14:15]
	v_lshl_add_u64 v[26:27], s[22:23], 0, v[196:197]
	v_lshl_add_u64 v[26:27], v[26:27], 0, v[14:15]
	global_load_dwordx4 v[70:73], v[24:25], off
	global_load_dwordx4 v[74:77], v[26:27], off
	s_add_i32 s33, s33, 64
	s_and_b32 s20, s33, 0x3c0
	s_lshl_b32 s0, s20, 2
	s_add_u32 s0, s25, s0
	s_addc_u32 s1, s26, 0
	v_lshl_add_u64 v[24:25], s[0:1], 0, v[180:181]
	v_lshl_add_u64 v[24:25], v[24:25], 0, v[182:183]
	s_lshl_b32 s20, s20, 1
	global_load_dwordx4 v[42:45], v[24:25], off offset:16
	global_load_dwordx4 v[46:49], v[24:25], off
	v_lshl_add_u64 v[24:25], s[0:1], 0, v[184:185]
	s_add_u32 s20, s27, s20
	v_lshl_add_u64 v[24:25], v[24:25], 0, v[182:183]
	s_addc_u32 s21, s28, 0
	global_load_dwordx4 v[34:37], v[24:25], off offset:16
	global_load_dwordx4 v[38:41], v[24:25], off
	v_lshl_add_u64 v[24:25], s[20:21], 0, v[186:187]
	v_lshl_add_u64 v[24:25], v[24:25], 0, v[14:15]
	v_lshl_add_u64 v[26:27], s[20:21], 0, v[188:189]
	v_lshl_add_u64 v[78:79], v[26:27], 0, v[14:15]
	global_load_dwordx4 v[30:33], v[24:25], off
	global_load_dwordx4 v[26:29], v[78:79], off
	s_waitcnt vmcnt(16)
	v_cvt_pk_bf16_f32 v6, v6, v7
	v_cvt_pk_bf16_f32 v7, v8, v9
	v_cvt_pk_bf16_f32 v8, v2, v3
	v_add_u32_e32 v2, 0, v208
	v_cvt_pk_bf16_f32 v9, v4, v5
	ds_write_b128 v2, v[6:9]
	s_waitcnt vmcnt(14)
	v_cvt_pk_bf16_f32 v2, v16, v17
	v_add_u32_e32 v6, 0, v205
	v_cvt_pk_bf16_f32 v3, v18, v19
	v_cvt_pk_bf16_f32 v4, v10, v11
	v_cvt_pk_bf16_f32 v5, v12, v13
	ds_write_b128 v6, v[2:5]
	v_add_u32_e32 v2, 0, v206
	s_waitcnt vmcnt(13)
	ds_write_b128 v2, v[20:23] offset:32768
	v_add_u32_e32 v2, 0, v207
	s_waitcnt vmcnt(12)
	ds_write_b128 v2, v[50:53] offset:32768
	s_waitcnt vmcnt(10)
	v_cvt_pk_bf16_f32 v2, v58, v59
	v_add_u32_e32 v6, 0, v204
	v_cvt_pk_bf16_f32 v3, v60, v61
	v_cvt_pk_bf16_f32 v4, v54, v55
	v_cvt_pk_bf16_f32 v5, v56, v57
	ds_write_b128 v6, v[2:5]
	s_waitcnt vmcnt(8)
	v_cvt_pk_bf16_f32 v2, v66, v67
	v_add_u32_e32 v6, 0, v201
	v_cvt_pk_bf16_f32 v3, v68, v69
	v_cvt_pk_bf16_f32 v4, v62, v63
	v_cvt_pk_bf16_f32 v5, v64, v65
	ds_write_b128 v6, v[2:5]
	v_add_u32_e32 v2, 0, v202
	s_waitcnt vmcnt(7)
	ds_write_b128 v2, v[70:73] offset:32768
	v_add_u32_e32 v2, 0, v203
	s_waitcnt vmcnt(6)
	ds_write_b128 v2, v[74:77] offset:32768
	v_lshl_add_u64 v[2:3], s[0:1], 0, v[190:191]
	v_lshl_add_u64 v[2:3], v[2:3], 0, v[182:183]
	global_load_dwordx4 v[6:9], v[2:3], off offset:16
	global_load_dwordx4 v[22:25], v[2:3], off
	v_lshl_add_u64 v[2:3], s[0:1], 0, v[192:193]
	v_lshl_add_u64 v[16:17], v[2:3], 0, v[182:183]
	global_load_dwordx4 v[2:5], v[16:17], off offset:16
	global_load_dwordx4 v[10:13], v[16:17], off
	v_lshl_add_u64 v[16:17], s[20:21], 0, v[194:195]
	v_lshl_add_u64 v[50:51], v[16:17], 0, v[14:15]
	v_lshl_add_u64 v[16:17], s[20:21], 0, v[196:197]
	v_lshl_add_u64 v[52:53], v[16:17], 0, v[14:15]
	global_load_dwordx4 v[18:21], v[50:51], off
	global_load_dwordx4 v[14:17], v[52:53], off
	v_lshlrev_b32_e32 v50, 13, v200
	s_cmp_lg_u32 0, -1
	s_cselect_b32 s0, 0, 0
	v_add3_u32 v209, v80, s0, v81
	s_add_i32 s0, s0, 0x8000
	v_add3_u32 v210, v50, s0, v81
	s_lshl_b32 s0, s30, 1
	s_add_i32 s31, s31, s0
	s_lshl_b32 s0, s2, 3
	s_add_i32 s0, s0, s31
	s_waitcnt lgkmcnt(0)
	s_and_b32 s0, s0, 15
	s_lshl_b32 s0, s0, 6
	s_add_i32 s22, s0, 0x80
	v_mov_b32_e32 v50, v183
	v_mov_b32_e32 v51, v183
	v_mov_b32_e32 v52, v183
	v_mov_b32_e32 v53, v183
	v_mov_b32_e32 v54, v183
	v_mov_b32_e32 v55, v183
	v_mov_b32_e32 v56, v183
	v_mov_b32_e32 v57, v183
	v_mov_b32_e32 v58, v183
	v_mov_b32_e32 v59, v183
	v_mov_b32_e32 v60, v183
	v_mov_b32_e32 v61, v183
	v_mov_b32_e32 v62, v183
	v_mov_b32_e32 v63, v183
	v_mov_b32_e32 v64, v183
	v_mov_b32_e32 v65, v183
	v_mov_b32_e32 v66, v183
	v_mov_b32_e32 v67, v183
	v_mov_b32_e32 v68, v183
	v_mov_b32_e32 v69, v183
	v_mov_b32_e32 v70, v183
	v_mov_b32_e32 v71, v183
	v_mov_b32_e32 v72, v183
	v_mov_b32_e32 v73, v183
	v_mov_b32_e32 v74, v183
	v_mov_b32_e32 v75, v183
	v_mov_b32_e32 v76, v183
	v_mov_b32_e32 v77, v183
	v_mov_b32_e32 v78, v183
	v_mov_b32_e32 v79, v183
	v_mov_b32_e32 v80, v183
	v_mov_b32_e32 v81, v183
	v_mov_b32_e32 v82, v183
	v_mov_b32_e32 v83, v183
	v_mov_b32_e32 v84, v183
	v_mov_b32_e32 v85, v183
	v_mov_b32_e32 v86, v183
	v_mov_b32_e32 v87, v183
	v_mov_b32_e32 v88, v183
	v_mov_b32_e32 v89, v183
	v_mov_b32_e32 v90, v183
	v_mov_b32_e32 v91, v183
	v_mov_b32_e32 v92, v183
	v_mov_b32_e32 v93, v183
	v_mov_b32_e32 v94, v183
	v_mov_b32_e32 v95, v183
	v_mov_b32_e32 v96, v183
	v_mov_b32_e32 v97, v183
	v_mov_b32_e32 v98, v183
	v_mov_b32_e32 v99, v183
	v_mov_b32_e32 v100, v183
	v_mov_b32_e32 v101, v183
	v_mov_b32_e32 v102, v183
	v_mov_b32_e32 v103, v183
	v_mov_b32_e32 v104, v183
	v_mov_b32_e32 v105, v183
	v_mov_b32_e32 v106, v183
	v_mov_b32_e32 v107, v183
	v_mov_b32_e32 v108, v183
	v_mov_b32_e32 v109, v183
	v_mov_b32_e32 v110, v183
	v_mov_b32_e32 v111, v183
	v_mov_b32_e32 v112, v183
	v_mov_b32_e32 v113, v183
	v_mov_b32_e32 v114, v183
	v_mov_b32_e32 v115, v183
	v_mov_b32_e32 v116, v183
	v_mov_b32_e32 v117, v183
	v_mov_b32_e32 v118, v183
	v_mov_b32_e32 v119, v183
	v_mov_b32_e32 v120, v183
	v_mov_b32_e32 v121, v183
	v_mov_b32_e32 v122, v183
	v_mov_b32_e32 v123, v183
	v_mov_b32_e32 v124, v183
	v_mov_b32_e32 v125, v183
	v_mov_b32_e32 v126, v183
	v_mov_b32_e32 v127, v183
	v_mov_b32_e32 v128, v183
	v_mov_b32_e32 v129, v183
	v_mov_b32_e32 v130, v183
	v_mov_b32_e32 v131, v183
	v_mov_b32_e32 v132, v183
	v_mov_b32_e32 v133, v183
	v_mov_b32_e32 v134, v183
	v_mov_b32_e32 v135, v183
	v_mov_b32_e32 v136, v183
	v_mov_b32_e32 v137, v183
	v_mov_b32_e32 v138, v183
	v_mov_b32_e32 v139, v183
	v_mov_b32_e32 v140, v183
	v_mov_b32_e32 v141, v183
	v_mov_b32_e32 v142, v183
	v_mov_b32_e32 v143, v183
	v_mov_b32_e32 v144, v183
	v_mov_b32_e32 v145, v183
	v_mov_b32_e32 v146, v183
	v_mov_b32_e32 v147, v183
	v_mov_b32_e32 v148, v183
	v_mov_b32_e32 v149, v183
	v_mov_b32_e32 v150, v183
	v_mov_b32_e32 v151, v183
	v_mov_b32_e32 v152, v183
	v_mov_b32_e32 v153, v183
	v_mov_b32_e32 v154, v183
	v_mov_b32_e32 v155, v183
	v_mov_b32_e32 v156, v183
	v_mov_b32_e32 v157, v183
	v_mov_b32_e32 v158, v183
	v_mov_b32_e32 v159, v183
	v_mov_b32_e32 v160, v183
	v_mov_b32_e32 v161, v183
	v_mov_b32_e32 v162, v183
	v_mov_b32_e32 v163, v183
	v_mov_b32_e32 v164, v183
	v_mov_b32_e32 v165, v183
	v_mov_b32_e32 v166, v183
	v_mov_b32_e32 v167, v183
	v_mov_b32_e32 v168, v183
	v_mov_b32_e32 v169, v183
	v_mov_b32_e32 v170, v183
	v_mov_b32_e32 v171, v183
	v_mov_b32_e32 v172, v183
	v_mov_b32_e32 v173, v183
	v_mov_b32_e32 v174, v183
	v_mov_b32_e32 v175, v183
	v_mov_b32_e32 v176, v183
	v_mov_b32_e32 v177, v183
	s_barrier
